# speedup vs baseline: 1.0660x; 1.0191x over previous
_Z7k_finalPKfPKiPf:
	s_load_dwordx4 s[4:7], s[0:1], 0x0
	s_load_dwordx2 s[8:9], s[0:1], 0x10
	s_mul_hi_u32 s3, s2, 0xaaaaaaab
	v_lshrrev_b32_e32 v1, 6, v0
	v_and_b32_e32 v2, 63, v0
	s_lshr_b32 s10, s3, 1
	s_mul_i32 s3, s10, 3
	s_sub_i32 s11, s2, s3
	s_mul_i32 s12, s10, 0xc000
	s_lshl_b32 s13, s11, 8
	s_add_u32 s12, s12, s13
	v_mul_u32_u24_e32 v3, 0x3000, v1
	v_lshl_add_u32 v3, v2, 2, v3
	v_add_u32_e32 v3, s12, v3
	v_add_u32_e32 v4, 0x1200, v3
	v_add_u32_e32 v5, 0x2400, v3
	v_lshlrev_b32_e32 v6, 2, v0
	v_lshlrev_b32_e32 v8, 2, v2
	v_mov_b32_e32 v9, 0
	v_readfirstlane_b32 s14, v1
	v_lshl_or_b32 v29, v1, 8, v8
	s_waitcnt lgkmcnt(0)
	global_load_dword v7, v6, s[6:7]
	global_load_dword v10, v3, s[4:5]
	global_load_dword v18, v3, s[4:5] offset:768
	global_load_dword v11, v3, s[4:5] offset:1536
	global_load_dword v19, v3, s[4:5] offset:2304
	global_load_dword v12, v3, s[4:5] offset:3072
	global_load_dword v20, v3, s[4:5] offset:3840
	global_load_dword v13, v4, s[4:5]
	global_load_dword v21, v4, s[4:5] offset:768
	global_load_dword v14, v4, s[4:5] offset:1536
	global_load_dword v22, v4, s[4:5] offset:2304
	global_load_dword v15, v4, s[4:5] offset:3072
	global_load_dword v23, v4, s[4:5] offset:3840
	global_load_dword v16, v5, s[4:5]
	global_load_dword v24, v5, s[4:5] offset:768
	global_load_dword v17, v5, s[4:5] offset:1536
	global_load_dword v25, v5, s[4:5] offset:2304
	s_lshl_b32 s19, s14, 3
	v_mov_b32_e32 v28, s19
	s_waitcnt vmcnt(16)
	s_nop 0
	v_add_u32_dpp v7, v7, v7 quad_perm:[1,0,3,2] row_mask:0xf bank_mask:0xf
	s_nop 1
	v_add_u32_dpp v7, v7, v7 quad_perm:[2,3,0,1] row_mask:0xf bank_mask:0xf
	s_nop 1
	v_add_u32_dpp v7, v7, v7 row_half_mirror row_mask:0xf bank_mask:0xf
	s_nop 1
	v_add_u32_dpp v7, v7, v7 row_mirror row_mask:0xf bank_mask:0xf
	s_nop 1
	v_readlane_b32 s15, v7, 0
	v_readlane_b32 s16, v7, 16
	v_readlane_b32 s17, v7, 32
	v_readlane_b32 s18, v7, 48
	s_add_u32 s15, s15, s16
	s_add_u32 s17, s17, s18
	v_mov_b32_e32 v26, s15
	v_mov_b32_e32 v27, s17
	s_mov_b64 exec, 1
	ds_write_b64 v28, v[26:27] offset:2048
	s_mov_b64 exec, -1
	s_waitcnt vmcnt(0)
	v_add_f32_e32 v10, v10, v11
	v_add_f32_e32 v12, v12, v13
	v_add_f32_e32 v14, v14, v15
	v_add_f32_e32 v16, v16, v17
	v_add_f32_e32 v18, v18, v19
	v_add_f32_e32 v20, v20, v21
	v_add_f32_e32 v22, v22, v23
	v_add_f32_e32 v24, v24, v25
	v_add_f32_e32 v10, v10, v12
	v_add_f32_e32 v14, v14, v16
	v_add_f32_e32 v18, v18, v20
	v_add_f32_e32 v22, v22, v24
	v_add_f32_e32 v10, v10, v14
	v_add_f32_e32 v18, v18, v22
	ds_write2st64_b32 v29, v10, v18 offset1:4
	s_waitcnt lgkmcnt(0)
	s_barrier
	s_cmp_lg_u32 s14, 0
	s_cbranch_scc1 .Lf_end
	ds_read2st64_b32 v[10:11], v8 offset1:1
	ds_read2st64_b32 v[12:13], v8 offset0:2 offset1:3
	ds_read2st64_b32 v[14:15], v8 offset0:4 offset1:5
	ds_read2st64_b32 v[16:17], v8 offset0:6 offset1:7
	ds_read_b32 v20, v8 offset:2048
	s_waitcnt lgkmcnt(1)
	v_add_f32_e32 v10, v10, v11
	v_add_f32_e32 v12, v12, v13
	v_add_f32_e32 v14, v14, v15
	v_add_f32_e32 v16, v16, v17
	v_add_f32_e32 v30, v10, v12
	v_add_f32_e32 v31, v14, v16
	s_waitcnt lgkmcnt(0)
	v_cmp_lt_i32_e64 s[20:21], 9, v20
	v_add_f32_dpp v32, v30, v30 quad_perm:[1,0,3,2] row_mask:0xf bank_mask:0xf
	v_add_f32_dpp v33, v31, v31 quad_perm:[1,0,3,2] row_mask:0xf bank_mask:0xf
	s_and_b32 s20, s20, 0xff
	s_bcnt1_i32_b32 s22, s20
	s_nop 0
	v_add_f32_dpp v32, v32, v32 quad_perm:[2,3,0,1] row_mask:0xf bank_mask:0xf
	v_add_f32_dpp v33, v33, v33 quad_perm:[2,3,0,1] row_mask:0xf bank_mask:0xf
	s_max_u32 s22, s22, 1
	s_mulk_i32 s22, 0xc0
	s_nop 0
	v_add_f32_dpp v32, v32, v32 row_half_mirror row_mask:0xf bank_mask:0xf
	v_add_f32_dpp v33, v33, v33 row_half_mirror row_mask:0xf bank_mask:0xf
	s_bitcmp1_b32 s20, s10
	s_cselect_b32 s23, 1.0, 0
	s_nop 0
	v_add_f32_dpp v32, v32, v32 row_mirror row_mask:0xf bank_mask:0xf
	v_add_f32_dpp v33, v33, v33 row_mirror row_mask:0xf bank_mask:0xf
	v_cvt_f32_u32_e32 v35, s22
	s_nop 0
	v_readlane_b32 s12, v32, 0
	v_readlane_b32 s13, v32, 16
	v_readlane_b32 s15, v32, 32
	v_readlane_b32 s16, v32, 48
	v_readlane_b32 s17, v33, 0
	v_readlane_b32 s18, v33, 16
	v_readlane_b32 s19, v33, 32
	v_readlane_b32 s24, v33, 48
	v_mov_b32_e32 v3, s13
	v_mov_b32_e32 v4, s16
	v_mov_b32_e32 v5, s18
	v_mov_b32_e32 v6, s24
	v_add_f32_e32 v3, s12, v3
	v_add_f32_e32 v4, s15, v4
	v_add_f32_e32 v5, s17, v5
	v_add_f32_e32 v6, s19, v6
	v_add_f32_e32 v3, v3, v4
	v_add_f32_e32 v5, v5, v6
	v_add_f32_e32 v3, 0x322bcc77, v3
	v_add_f32_e32 v5, 0x322bcc77, v5
	v_div_scale_f32 v10, s[12:13], v3, v3, v30
	v_div_scale_f32 v11, s[12:13], v5, v5, v31
	v_rcp_f32_e32 v12, v10
	v_rcp_f32_e32 v13, v11
	v_div_scale_f32 v14, vcc, v30, v3, v30
	v_div_scale_f32 v15, s[16:17], v31, v5, v31
	v_fma_f32 v16, -v10, v12, 1.0
	v_fma_f32 v17, -v11, v13, 1.0
	v_fmac_f32_e32 v12, v16, v12
	v_fmac_f32_e32 v13, v17, v13
	v_mul_f32_e32 v16, v14, v12
	v_mul_f32_e32 v17, v15, v13
	v_fma_f32 v18, -v10, v16, v14
	v_fma_f32 v19, -v11, v17, v15
	v_fmac_f32_e32 v16, v18, v12
	v_fmac_f32_e32 v17, v19, v13
	v_fma_f32 v10, -v10, v16, v14
	v_fma_f32 v11, -v11, v17, v15
	v_div_fmas_f32 v10, v10, v12, v16
	s_mov_b64 vcc, s[16:17]
	s_nop 3
	v_div_fmas_f32 v11, v11, v13, v17
	v_div_fixup_f32 v10, v10, v3, v30
	v_div_fixup_f32 v11, v11, v5, v31
	v_sub_f32_e32 v10, v10, v11
	v_and_b32_e32 v11, 0x7fffffff, v10
	s_nop 1
	v_add_f32_dpp v10, v11, |v10| quad_perm:[1,0,3,2] row_mask:0xf bank_mask:0xf
	s_nop 1
	v_add_f32_dpp v10, v10, v10 quad_perm:[2,3,0,1] row_mask:0xf bank_mask:0xf
	s_nop 1
	v_add_f32_dpp v10, v10, v10 row_half_mirror row_mask:0xf bank_mask:0xf
	s_nop 1
	v_add_f32_dpp v10, v10, v10 row_mirror row_mask:0xf bank_mask:0xf
	s_nop 1
	v_readlane_b32 s12, v10, 0
	v_readlane_b32 s13, v10, 16
	v_readlane_b32 s15, v10, 32
	v_readlane_b32 s16, v10, 48
	s_mov_b64 exec, 1
	v_mov_b32_e32 v3, s13
	v_mov_b32_e32 v4, s16
	v_add_f32_e32 v3, s12, v3
	v_add_f32_e32 v4, s15, v4
	v_add_f32_e32 v3, v3, v4
	v_mul_f32_e32 v3, s23, v3
	v_div_scale_f32 v4, s[12:13], v35, v35, v3
	v_rcp_f32_e32 v5, v4
	v_div_scale_f32 v6, vcc, v3, v35, v3
	v_fma_f32 v7, -v4, v5, 1.0
	v_fmac_f32_e32 v5, v7, v5
	v_mul_f32_e32 v7, v6, v5
	v_fma_f32 v10, -v4, v7, v6
	v_fmac_f32_e32 v7, v10, v5
	v_fma_f32 v4, -v4, v7, v6
	v_div_fmas_f32 v4, v4, v5, v7
	v_div_fixup_f32 v3, v4, v35, v3
	global_atomic_add_f32 v9, v3, s[8:9]

	.amdhsa_kernel _Z7k_finalPKfPKiPf
		.amdhsa_group_segment_fixed_size 2080
		.amdhsa_private_segment_fixed_size 0
		.amdhsa_kernarg_size 24
		.amdhsa_user_sgpr_count 2
		.amdhsa_user_sgpr_dispatch_ptr 0
		.amdhsa_user_sgpr_queue_ptr 0
		.amdhsa_user_sgpr_kernarg_segment_ptr 1
		.amdhsa_user_sgpr_dispatch_id 0
		.amdhsa_user_sgpr_kernarg_preload_length 0
		.amdhsa_user_sgpr_kernarg_preload_offset 0
		.amdhsa_user_sgpr_private_segment_size 0
		.amdhsa_uses_dynamic_stack 0
		.amdhsa_enable_private_segment 0
		.amdhsa_system_sgpr_workgroup_id_x 1
		.amdhsa_system_sgpr_workgroup_id_y 0
		.amdhsa_system_sgpr_workgroup_id_z 0
		.amdhsa_system_sgpr_workgroup_info 0
		.amdhsa_system_vgpr_workitem_id 0
		.amdhsa_next_free_vgpr 36
		.amdhsa_next_free_sgpr 28
		.amdhsa_accum_offset 36
		.amdhsa_reserve_vcc 1
		.amdhsa_float_round_mode_32 0
		.amdhsa_float_round_mode_16_64 0
		.amdhsa_float_denorm_mode_32 3
		.amdhsa_float_denorm_mode_16_64 3
		.amdhsa_dx10_clamp 1
		.amdhsa_ieee_mode 1
		.amdhsa_fp16_overflow 0
		.amdhsa_tg_split 0
		.amdhsa_exception_fp_ieee_invalid_op 0
		.amdhsa_exception_fp_denorm_src 0
		.amdhsa_exception_fp_ieee_div_zero 0
		.amdhsa_exception_fp_ieee_overflow 0
		.amdhsa_exception_fp_ieee_underflow 0
		.amdhsa_exception_fp_ieee_inexact 0
		.amdhsa_exception_int_div_zero 0
	.end_amdhsa_kernel

.Lfunc_end1:
	.size	_Z7k_finalPKfPKiPf, .Lfunc_end1-_Z7k_finalPKfPKiPf
	.set _Z7k_finalPKfPKiPf.num_vgpr, 36
	.set _Z7k_finalPKfPKiPf.num_agpr, 0
	.set _Z7k_finalPKfPKiPf.numbered_sgpr, 28
	.set _Z7k_finalPKfPKiPf.num_named_barrier, 0
	.set _Z7k_finalPKfPKiPf.private_seg_size, 0
	.set _Z7k_finalPKfPKiPf.uses_vcc, 1
	.set _Z7k_finalPKfPKiPf.uses_flat_scratch, 0
	.set _Z7k_finalPKfPKiPf.has_dyn_sized_stack, 0
	.set _Z7k_finalPKfPKiPf.has_recursion, 0
	.set _Z7k_finalPKfPKiPf.has_indirect_call, 0

amdhsa.kernels:
  - .agpr_count:     0
    .args:
      - .actual_access:  read_only
        .address_space:  global
        .offset:         0
        .size:           8
        .value_kind:     global_buffer
      - .actual_access:  read_only
        .address_space:  global
        .offset:         8
        .size:           8
        .value_kind:     global_buffer
      - .actual_access:  read_only
        .address_space:  global
        .offset:         16
        .size:           8
        .value_kind:     global_buffer
      - .actual_access:  write_only
        .address_space:  global
        .offset:         24
        .size:           8
        .value_kind:     global_buffer
      - .actual_access:  write_only
        .address_space:  global
        .offset:         32
        .size:           8
        .value_kind:     global_buffer
      - .actual_access:  write_only
        .address_space:  global
        .offset:         40
        .size:           8
        .value_kind:     global_buffer
    .group_segment_fixed_size: 32
    .kernarg_segment_align: 8
    .kernarg_segment_size: 48
    .language:       OpenCL C
    .language_version:
      - 2
      - 0
    .max_flat_workgroup_size: 1024
    .name:           _Z6k_histPKfS0_S0_PfPiS1_
    .private_segment_fixed_size: 0
    .sgpr_count:     66
    .sgpr_spill_count: 0
    .symbol:         _Z6k_histPKfS0_S0_PfPiS1_.kd
    .uniform_work_group_size: 1
    .uses_dynamic_stack: false
    .vgpr_count:     50
    .vgpr_spill_count: 0
    .wavefront_size: 64
  - .agpr_count:     0
    .args:
      - .actual_access:  read_only
        .address_space:  global
        .offset:         0
        .size:           8
        .value_kind:     global_buffer
      - .actual_access:  read_only
        .address_space:  global
        .offset:         8
        .size:           8
        .value_kind:     global_buffer
      - .address_space:  global
        .offset:         16
        .size:           8
        .value_kind:     global_buffer
    .group_segment_fixed_size: 2080
    .kernarg_segment_align: 8
    .kernarg_segment_size: 24
    .language:       OpenCL C
    .language_version:
      - 2
      - 0
    .max_flat_workgroup_size: 256
    .name:           _Z7k_finalPKfPKiPf
    .private_segment_fixed_size: 0
    .sgpr_count:     34
    .sgpr_spill_count: 0
    .symbol:         _Z7k_finalPKfPKiPf.kd
    .uniform_work_group_size: 1
    .uses_dynamic_stack: false
    .vgpr_count:     36
    .vgpr_spill_count: 0
    .wavefront_size: 64
